# P0 order split plus a ~50 us start delay of the sections-first workgroups before they begin streaming expert weights (fewer concurrent HBM streams)
# speedup vs baseline: 1.0028x; 1.0028x over previous
.LBB0_205:
	s_cmp_eq_u32 s101, 2
	s_cbranch_scc1 .Lp0_end
	s_cmp_lg_u32 s101, 0
	s_cbranch_scc1 .Lp0_nodly
	s_mov_b32 s100, 13
.Lp0_dly:
	s_sleep 127
	s_sub_u32 s100, s100, 1
	s_cmp_lg_u32 s100, 0
	s_cbranch_scc1 .Lp0_dly
